# speedup vs baseline: 1.0327x; 1.0010x over previous
.LBB2_79:
	v_lshrrev_b32_e32 v2, 2, v0
	v_and_b32_e32 v3, 3, v0
	s_add_i32 s21, 0, 0x16000
	v_mul_u32_u24_e32 v2, 0x90, v2
	v_lshlrev_b32_e32 v160, 2, v3
	v_add3_u32 v2, s21, v2, v160
	v_add_u32_e32 v2, 0x80, v2
	s_waitcnt vmcnt(11)
	ds_write2st64_b32 v2, v8, v9 offset1:72
	v_permlane32_swap_b32_e32 v110, v112
	v_permlane32_swap_b32_e32 v111, v113
	v_permlane32_swap_b32_e32 v106, v108
	v_permlane32_swap_b32_e32 v107, v109
	v_permlane32_swap_b32_e32 v102, v104
	v_permlane32_swap_b32_e32 v103, v105
	v_permlane32_swap_b32_e32 v98, v100
	v_permlane32_swap_b32_e32 v99, v101
	v_lshl_add_u32 v125, v4, 1, 0
	s_waitcnt vmcnt(8)
	s_waitcnt lgkmcnt(0)
	s_barrier
	ds_read_b128 v[2:5], v125
	ds_read_b128 v[18:21], v125 offset:1024
	s_waitcnt lgkmcnt(1)
	v_mfma_f32_32x32x16_f16 v[2:17], v[2:5], v[110:113], 0
	v_mul_u32_u24_e32 v165, 0x48, v164
	v_lshl_add_u32 v173, v165, 1, s21
	s_mul_i32 s18, s28, 0x4800
	s_add_i32 s18, s21, s18
	s_movk_i32 s23, 0x90
	v_lshlrev_b32_e32 v69, 4, v164
	s_mul_i32 s20, s28, 0x4400
	s_waitcnt lgkmcnt(0)
	v_mfma_f32_32x32x16_f16 v[2:17], v[18:21], v[106:109], v[2:17]
	ds_read_b128 v[18:21], v125 offset:2048
	ds_read_b128 v[22:25], v125 offset:3072
	ds_read_b128 v[34:37], v125 offset:9216
	ds_read_b128 v[38:41], v125 offset:10240
	s_add_i32 s20, s20, 0
	s_add_i32 s20, s20, 0x1f000
	s_lshl_b32 s15, s15, 1
	s_add_i32 s15, s20, s15
	s_waitcnt lgkmcnt(3)
	v_mfma_f32_32x32x16_f16 v[2:17], v[18:21], v[102:105], v[2:17]
	ds_read_b128 v[18:21], v125 offset:8192
	ds_read_b128 v[72:75], v125 offset:4096
	ds_read_b128 v[76:79], v125 offset:5120
	v_add_u32_e32 v167, s15, v69
	s_movk_i32 s15, 0x110
	s_load_dwordx8 s[4:11], s[0:1], 0x88
	v_lshlrev_b32_e32 v126, 2, v164
	s_mov_b32 s19, 0
	s_waitcnt lgkmcnt(0)
	v_mfma_f32_32x32x16_f16 v[2:17], v[22:25], v[98:101], v[2:17]
	s_and_b64 vcc, exec, s[2:3]
	v_mfma_f32_32x32x16_f16 v[18:33], v[18:21], v[110:113], 0
	v_mfma_f32_32x32x16_f16 v[18:33], v[34:37], v[106:109], v[18:33]
	ds_read_b128 v[80:83], v173 offset:128
	ds_read_b128 v[34:37], v125 offset:11264
	ds_read_b128 v[84:87], v125 offset:6144
	ds_read_b128 v[88:91], v125 offset:7168
	ds_read_b128 v[92:95], v173 offset:416
	s_waitcnt lgkmcnt(4)
	s_nop 2
	v_fmamk_f32 v68, v80, 0x3eb8aa3b, v2
	v_fmamk_f32 v70, v81, 0x3eb8aa3b, v3
	v_fmamk_f32 v4, v82, 0x3eb8aa3b, v4
	v_mfma_f32_32x32x16_f16 v[18:33], v[38:41], v[102:105], v[18:33]
	ds_read_b128 v[114:117], v173 offset:704
	ds_read_b128 v[128:131], v173 offset:992
	ds_read_b128 v[38:41], v125 offset:12288
	ds_read_b128 v[62:65], v173 offset:1280
	ds_read_b128 v[58:61], v173 offset:1568
	ds_read_b128 v[54:57], v173 offset:1856
	ds_read_b128 v[50:53], v173 offset:2144
	ds_read_b128 v[132:135], v125 offset:13312
	ds_read_b128 v[136:139], v173 offset:2432
	ds_read_b128 v[140:143], v125 offset:14336
	ds_read_b128 v[144:147], v125 offset:15360
	ds_read_b128 v[148:151], v173 offset:2720
	v_fmamk_f32 v5, v83, 0x3eb8aa3b, v5
	s_waitcnt lgkmcnt(12)
	v_fmamk_f32 v6, v92, 0x3eb8aa3b, v6
	v_fmamk_f32 v7, v93, 0x3eb8aa3b, v7
	v_fmamk_f32 v8, v94, 0x3eb8aa3b, v8
	v_mfma_f32_32x32x16_f16 v[18:33], v[34:37], v[98:101], v[18:33]
	v_fmamk_f32 v9, v95, 0x3eb8aa3b, v9
	s_waitcnt lgkmcnt(11)
	v_fmamk_f32 v10, v114, 0x3eb8aa3b, v10
	v_fmamk_f32 v11, v115, 0x3eb8aa3b, v11
	v_fmamk_f32 v12, v116, 0x3eb8aa3b, v12
	v_fmamk_f32 v13, v117, 0x3eb8aa3b, v13
	s_waitcnt lgkmcnt(10)
	v_fmamk_f32 v14, v128, 0x3eb8aa3b, v14
	v_fmamk_f32 v15, v129, 0x3eb8aa3b, v15
	s_waitcnt lgkmcnt(9)
	v_mfma_f32_32x32x16_f16 v[34:49], v[38:41], v[110:113], 0
	s_waitcnt lgkmcnt(3)
	v_add_f32_e32 v2, v18, v136
	v_add_f32_e32 v3, v19, v137
	v_add_f32_e32 v71, v20, v138
	v_add_f32_e32 v80, v21, v139
	ds_read_b128 v[18:21], v173 offset:3008
	s_waitcnt lgkmcnt(1)
	v_add_f32_e32 v81, v22, v148
	v_add_f32_e32 v96, v23, v149
	v_mfma_f32_32x32x16_f16 v[34:49], v[132:135], v[106:109], v[34:49]
	v_add_f32_e32 v97, v24, v150
	v_add_f32_e32 v122, v25, v151
	ds_read_b128 v[22:25], v173 offset:3296
	s_waitcnt lgkmcnt(1)
	v_add_f32_e32 v123, v26, v18
	v_add_f32_e32 v127, v27, v19
	v_add_f32_e32 v132, v28, v20
	v_add_f32_e32 v133, v29, v21
	v_mfma_f32_32x32x16_f16 v[34:49], v[140:143], v[102:105], v[34:49]
	s_waitcnt lgkmcnt(0)
	v_add_f32_e32 v134, v30, v22
	v_add_f32_e32 v135, v31, v23
	v_add_f32_e32 v136, v32, v24
	v_add_f32_e32 v137, v33, v25
	ds_read_b128 v[18:21], v173 offset:3584
	ds_read_b128 v[22:25], v173 offset:3872
	v_fmamk_f32 v16, v130, 0x3eb8aa3b, v16
	v_fmac_f32_e32 v17, 0x3eb8aa3b, v131
	v_mfma_f32_32x32x16_f16 v[34:49], v[144:147], v[98:101], v[34:49]
	s_waitcnt lgkmcnt(1)
	s_nop 10
	v_add_f32_e32 v138, v34, v18
	v_add_f32_e32 v139, v35, v19
	v_add_f32_e32 v140, v36, v20
	v_add_f32_e32 v141, v37, v21
	s_waitcnt lgkmcnt(0)
	v_add_f32_e32 v38, v38, v22
	ds_read_b128 v[18:21], v173 offset:4160
	v_add_f32_e32 v39, v39, v23
	v_add_f32_e32 v40, v40, v24
	v_add_f32_e32 v41, v41, v25
	ds_read_b128 v[22:25], v173 offset:4448
	v_mov_b32_e32 v34, s18
	v_mad_u32_u24 v34, v1, s23, v34
	v_add_u32_e32 v166, v34, v69
	v_cvt_pkrtz_f16_f32 v34, v2, v3
	v_cvt_pkrtz_f16_f32 v35, v71, v80
	v_cvt_pkrtz_f16_f32 v36, v81, v96
	v_cvt_pkrtz_f16_f32 v37, v97, v122
	ds_write_b128 v166, v[34:37]
	v_cvt_pkrtz_f16_f32 v34, v123, v127
	v_cvt_pkrtz_f16_f32 v35, v132, v133
	v_cvt_pkrtz_f16_f32 v36, v134, v135
	v_cvt_pkrtz_f16_f32 v37, v136, v137
	s_waitcnt lgkmcnt(2)
	v_add_f32_e32 v42, v42, v18
	v_add_f32_e32 v43, v43, v19
	v_add_f32_e32 v44, v44, v20
	v_add_f32_e32 v45, v45, v21
	s_waitcnt lgkmcnt(1)
	v_add_f32_e32 v46, v46, v22
	v_add_f32_e32 v47, v47, v23
	v_add_f32_e32 v48, v48, v24
	v_add_f32_e32 v49, v49, v25
	ds_write_b128 v166, v[34:37] offset:32
	v_cvt_pkrtz_f16_f32 v34, v138, v139
	v_cvt_pkrtz_f16_f32 v35, v140, v141
	v_cvt_pkrtz_f16_f32 v36, v38, v39
	v_cvt_pkrtz_f16_f32 v37, v40, v41
	ds_write_b128 v166, v[34:37] offset:64
	v_cvt_pkrtz_f16_f32 v34, v42, v43
	v_cvt_pkrtz_f16_f32 v35, v44, v45
	v_cvt_pkrtz_f16_f32 v36, v46, v47
	v_cvt_pkrtz_f16_f32 v37, v48, v49
	ds_write_b128 v166, v[34:37] offset:96
	ds_read_b128 v[34:37], v125 offset:16384
	v_lshrrev_b32_e32 v2, 2, v174
	v_mul_u32_u24_e32 v2, 0x48, v2
	v_lshlrev_b32_e32 v168, 1, v2
	v_add3_u32 v2, s21, v168, v160
	v_mfma_f32_32x32x16_f16 v[18:33], v[72:75], v[110:113], 0
	ds_read_b32 v2, v2 offset:4736
	ds_read_b128 v[72:75], v125 offset:17408
	v_mad_u32_u24 v71, v174, s15, v167
	s_waitcnt lgkmcnt(2)
	v_mfma_f32_32x32x16_f16 v[34:49], v[110:113], v[34:37], 0
	v_mfma_f32_32x32x16_f16 v[18:33], v[76:79], v[106:109], v[18:33]
	ds_read_b128 v[76:79], v125 offset:19456
	s_waitcnt lgkmcnt(1)
	v_mfma_f32_32x32x16_f16 v[34:49], v[106:109], v[72:75], v[34:49]
	ds_read_b128 v[72:75], v125 offset:18432
	s_waitcnt lgkmcnt(0)
	v_mfma_f32_32x32x16_f16 v[34:49], v[102:105], v[72:75], v[34:49]
	v_mfma_f32_32x32x16_f16 v[34:49], v[98:101], v[76:79], v[34:49]
	v_mfma_f32_32x32x16_f16 v[18:33], v[84:87], v[102:105], v[18:33]
	s_nop 10
	v_add_f32_e32 v3, v2, v34
	v_add_f32_e32 v34, v2, v35
	v_add_f32_e32 v35, v2, v36
	v_add_f32_e32 v36, v2, v37
	v_add_f32_e32 v37, v2, v38
	v_add_f32_e32 v38, v2, v39
	v_add_f32_e32 v39, v2, v40
	v_add_f32_e32 v40, v2, v41
	v_add_f32_e32 v41, v2, v42
	v_add_f32_e32 v42, v2, v43
	v_add_f32_e32 v43, v2, v44
	v_add_f32_e32 v44, v2, v45
	v_add_f32_e32 v45, v2, v46
	v_add_f32_e32 v46, v2, v47
	v_add_f32_e32 v47, v2, v48
	v_add_f32_e32 v2, v2, v49
	v_cvt_pkrtz_f16_f32 v34, v3, v34
	v_cvt_pkrtz_f16_f32 v35, v35, v36
	v_cvt_pkrtz_f16_f32 v36, v37, v38
	v_cvt_pkrtz_f16_f32 v37, v39, v40
	ds_write_b128 v71, v[34:37]
	v_cvt_pkrtz_f16_f32 v34, v41, v42
	v_cvt_pkrtz_f16_f32 v35, v43, v44
	v_cvt_pkrtz_f16_f32 v36, v45, v46
	v_cvt_pkrtz_f16_f32 v37, v47, v2
	ds_write_b128 v71, v[34:37] offset:32
	ds_read_b128 v[34:37], v125 offset:20480
	v_or_b32_e32 v2, 32, v174
	v_lshrrev_b32_e32 v2, 2, v2
	v_mul_u32_u24_e32 v2, 0x48, v2
	v_lshlrev_b32_e32 v169, 1, v2
	v_add3_u32 v2, s21, v169, v160
	v_mfma_f32_32x32x16_f16 v[18:33], v[88:91], v[98:101], v[18:33]
	ds_read_b32 v2, v2 offset:4736
	ds_read_b128 v[72:75], v125 offset:21504
	s_waitcnt lgkmcnt(2)
	v_mfma_f32_32x32x16_f16 v[34:49], v[110:113], v[34:37], 0
	s_nop 7
	v_fmamk_f32 v26, v54, 0x3eb8aa3b, v26
	v_fmamk_f32 v27, v55, 0x3eb8aa3b, v27
	v_fmamk_f32 v28, v56, 0x3eb8aa3b, v28
	v_fmamk_f32 v29, v57, 0x3eb8aa3b, v29
	ds_read_b128 v[54:57], v125 offset:22528
	v_fmamk_f32 v22, v58, 0x3eb8aa3b, v22
	v_fmamk_f32 v23, v59, 0x3eb8aa3b, v23
	s_waitcnt lgkmcnt(1)
	v_mfma_f32_32x32x16_f16 v[34:49], v[106:109], v[72:75], v[34:49]
	v_fmamk_f32 v24, v60, 0x3eb8aa3b, v24
	v_fmamk_f32 v25, v61, 0x3eb8aa3b, v25
	ds_read_b128 v[58:61], v125 offset:23552
	v_fmamk_f32 v18, v62, 0x3eb8aa3b, v18
	v_fmamk_f32 v19, v63, 0x3eb8aa3b, v19
	v_fmamk_f32 v20, v64, 0x3eb8aa3b, v20
	v_fmamk_f32 v21, v65, 0x3eb8aa3b, v21
	s_waitcnt lgkmcnt(1)
	v_mfma_f32_32x32x16_f16 v[34:49], v[102:105], v[54:57], v[34:49]
	v_fmamk_f32 v30, v50, 0x3eb8aa3b, v30
	v_fmamk_f32 v31, v51, 0x3eb8aa3b, v31
	v_fmamk_f32 v32, v52, 0x3eb8aa3b, v32
	v_fmac_f32_e32 v33, 0x3eb8aa3b, v53
	s_waitcnt lgkmcnt(0)
	v_mfma_f32_32x32x16_f16 v[34:49], v[98:101], v[58:61], v[34:49]
	s_nop 11
	v_add_f32_e32 v3, v2, v34
	v_add_f32_e32 v34, v2, v35
	v_add_f32_e32 v35, v2, v36
	v_add_f32_e32 v36, v2, v37
	v_add_f32_e32 v37, v2, v38
	v_add_f32_e32 v38, v2, v39
	v_add_f32_e32 v39, v2, v40
	v_add_f32_e32 v40, v2, v41
	v_add_f32_e32 v41, v2, v42
	v_add_f32_e32 v42, v2, v43
	v_add_f32_e32 v43, v2, v44
	v_add_f32_e32 v44, v2, v45
	v_add_f32_e32 v45, v2, v46
	v_add_f32_e32 v46, v2, v47
	v_add_f32_e32 v47, v2, v48
	v_add_f32_e32 v2, v2, v49
	v_cvt_pkrtz_f16_f32 v34, v3, v34
	v_cvt_pkrtz_f16_f32 v35, v35, v36
	v_cvt_pkrtz_f16_f32 v36, v37, v38
	v_cvt_pkrtz_f16_f32 v37, v39, v40
	ds_write_b128 v71, v[34:37] offset:8704
	v_cvt_pkrtz_f16_f32 v34, v41, v42
	v_cvt_pkrtz_f16_f32 v35, v43, v44
	v_cvt_pkrtz_f16_f32 v36, v45, v46
	v_cvt_pkrtz_f16_f32 v37, v47, v2
	ds_write_b128 v71, v[34:37] offset:8736
	s_waitcnt vmcnt(0) lgkmcnt(0)
	s_barrier
	s_cbranch_vccz .LBB2_82
	s_lshl_b32 s2, s22, 10
	s_add_i32 s23, s2, 0
	s_lshl_b64 s[2:3], s[14:15], 4
	s_add_i32 s21, s22, -8
	s_and_b32 s3, s3, 15
	s_and_b32 s2, s2, 0xfffffc00
	s_add_u32 s2, s16, s2
	s_addc_u32 s3, s17, s3
	v_lshl_add_u64 v[2:3], v[120:121], 1, s[2:3]
	s_mov_b64 s[2:3], 0x30000
	v_lshl_add_u64 v[2:3], v[2:3], 0, s[2:3]
	s_mov_b64 s[2:3], 0x2000

.LBB4_43:
	s_or_b64 exec, exec, s[2:3]
	v_lshlrev_b32_e32 v42, 4, v44
	v_mov_b32_e32 v43, 0
	s_waitcnt vmcnt(6)
	s_waitcnt lgkmcnt(0)
	s_barrier
	s_load_dwordx4 s[8:11], s[0:1], 0x88
	s_andn2_b64 vcc, exec, s[4:5]
	v_mbcnt_lo_u32_b32 v43, -1, 0
	s_cbranch_vccnz .LBB4_47
	v_mbcnt_hi_u32_b32 v7, -1, v43
	v_and_b32_e32 v6, 64, v7
	v_add_u32_e32 v10, 64, v6
	v_xor_b32_e32 v6, 1, v7
	v_cmp_lt_i32_e32 vcc, v6, v10
	v_xor_b32_e32 v9, 2, v7
	v_xor_b32_e32 v16, 32, v7
	v_cndmask_b32_e32 v6, v7, v6, vcc
	v_lshlrev_b32_e32 v11, 2, v6
	ds_bpermute_b32 v6, v11, v3
	v_cmp_lt_i32_e32 vcc, v9, v10
	v_add_u32_e32 v5, v80, v81
	v_add3_u32 v5, v5, v82, v83
	v_add3_u32 v5, v5, v84, v85
	v_add3_u32 v5, v5, v86, v87
	v_cvt_f32_i32_e32 v19, v5
	s_mov_b32 s13, 0x800000
	s_mov_b32 s12, 0x3f317217
	s_waitcnt lgkmcnt(0)
	v_add_f32_e32 v3, v3, v6
	v_cndmask_b32_e32 v6, v7, v9, vcc
	v_lshlrev_b32_e32 v12, 2, v6
	ds_bpermute_b32 v6, v12, v3
	v_xor_b32_e32 v9, 4, v7
	v_cmp_lt_i32_e32 vcc, v9, v10
	s_mov_b32 s14, 0x7f800000
	s_waitcnt lgkmcnt(0)
	v_add_f32_e32 v3, v3, v6
	v_cndmask_b32_e32 v6, v7, v9, vcc
	v_lshlrev_b32_e32 v13, 2, v6
	ds_bpermute_b32 v6, v13, v3
	v_xor_b32_e32 v9, 8, v7
	v_cmp_lt_i32_e32 vcc, v9, v10
	s_waitcnt lgkmcnt(0)
	v_add_f32_e32 v3, v3, v6
	v_cndmask_b32_e32 v6, v7, v9, vcc
	v_lshlrev_b32_e32 v14, 2, v6
	ds_bpermute_b32 v6, v14, v3
	v_xor_b32_e32 v9, 16, v7
	v_cmp_lt_i32_e32 vcc, v9, v10
	s_waitcnt lgkmcnt(0)
	v_add_f32_e32 v3, v3, v6
	v_cndmask_b32_e32 v6, v7, v9, vcc
	v_lshlrev_b32_e32 v15, 2, v6
	ds_bpermute_b32 v9, v15, v3
	v_cmp_lt_i32_e32 vcc, v16, v10
	ds_bpermute_b32 v6, v11, v2
	s_waitcnt lgkmcnt(0)
	v_add_f32_e32 v9, v3, v9
	v_lshlrev_b32_e32 v3, 2, v7
	v_and_b32_e32 v3, 0x100, v3
	v_cndmask_b32_e32 v10, v7, v16, vcc
	ds_bpermute_b32 v7, v3, v8
	ds_bpermute_b32 v16, v3, v5
	ds_bpermute_b32 v17, v3, v8 offset:4
	ds_bpermute_b32 v18, v3, v5 offset:4
	ds_bpermute_b32 v20, v3, v8 offset:12
	s_waitcnt lgkmcnt(0)
	v_cmp_eq_u32_e32 vcc, v7, v44
	ds_bpermute_b32 v21, v3, v5 offset:12
	ds_bpermute_b32 v22, v3, v5 offset:20
	v_cndmask_b32_e32 v7, 0, v16, vcc
	v_cmp_eq_u32_e32 vcc, v17, v44
	ds_bpermute_b32 v17, v3, v8 offset:8
	s_nop 0
	v_cndmask_b32_e32 v16, 0, v18, vcc
	ds_bpermute_b32 v18, v3, v5 offset:8
	v_add_u32_e32 v7, v16, v7
	s_waitcnt lgkmcnt(0)
	v_cmp_eq_u32_e32 vcc, v17, v44
	s_nop 1
	v_cndmask_b32_e32 v16, 0, v18, vcc
	ds_bpermute_b32 v18, v3, v8 offset:16
	v_cmp_eq_u32_e32 vcc, v20, v44
	ds_bpermute_b32 v20, v3, v5 offset:16
	s_nop 0
	v_cndmask_b32_e32 v17, 0, v21, vcc
	ds_bpermute_b32 v21, v3, v8 offset:20
	s_waitcnt lgkmcnt(0)
	v_cmp_eq_u32_e32 vcc, v18, v44
	ds_bpermute_b32 v18, v3, v8 offset:24
	v_add3_u32 v7, v7, v16, v17
	v_cndmask_b32_e32 v16, 0, v20, vcc
	ds_bpermute_b32 v20, v3, v5 offset:24
	v_cmp_eq_u32_e32 vcc, v21, v44
	ds_bpermute_b32 v21, v3, v8 offset:28
	s_nop 0
	v_cndmask_b32_e32 v17, 0, v22, vcc
	ds_bpermute_b32 v22, v3, v5 offset:28
	s_waitcnt lgkmcnt(0)
	v_cmp_eq_u32_e32 vcc, v18, v44
	ds_bpermute_b32 v18, v3, v8 offset:32
	v_add3_u32 v7, v7, v16, v17
	v_cndmask_b32_e32 v16, 0, v20, vcc
	ds_bpermute_b32 v20, v3, v5 offset:32
	v_cmp_eq_u32_e32 vcc, v21, v44
	ds_bpermute_b32 v21, v3, v8 offset:36
	s_nop 0
	v_cndmask_b32_e32 v17, 0, v22, vcc
	ds_bpermute_b32 v22, v3, v5 offset:36
	s_waitcnt lgkmcnt(0)
	v_cmp_eq_u32_e32 vcc, v18, v44
	ds_bpermute_b32 v18, v3, v8 offset:40
	v_add3_u32 v7, v7, v16, v17
	v_cndmask_b32_e32 v16, 0, v20, vcc
	ds_bpermute_b32 v20, v3, v5 offset:40
	v_cmp_eq_u32_e32 vcc, v21, v44
	ds_bpermute_b32 v21, v3, v8 offset:44
	s_nop 0
	v_cndmask_b32_e32 v17, 0, v22, vcc
	ds_bpermute_b32 v22, v3, v5 offset:44
	s_waitcnt lgkmcnt(0)
	v_cmp_eq_u32_e32 vcc, v18, v44
	ds_bpermute_b32 v18, v3, v8 offset:48
	v_add3_u32 v7, v7, v16, v17
	v_cndmask_b32_e32 v16, 0, v20, vcc
	ds_bpermute_b32 v20, v3, v5 offset:48
	v_cmp_eq_u32_e32 vcc, v21, v44
	ds_bpermute_b32 v21, v3, v8 offset:52
	s_nop 0
	v_cndmask_b32_e32 v17, 0, v22, vcc
	ds_bpermute_b32 v22, v3, v5 offset:52
	s_waitcnt lgkmcnt(0)
	v_cmp_eq_u32_e32 vcc, v18, v44
	ds_bpermute_b32 v18, v3, v8 offset:56
	v_add3_u32 v7, v7, v16, v17
	v_cndmask_b32_e32 v16, 0, v20, vcc
	ds_bpermute_b32 v20, v3, v5 offset:56
	ds_bpermute_b32 v8, v3, v8 offset:60
	ds_bpermute_b32 v3, v3, v5 offset:60
	v_cmp_eq_u32_e32 vcc, v21, v44
	s_nop 1
	v_cndmask_b32_e32 v17, 0, v22, vcc
	s_waitcnt lgkmcnt(0)
	v_cmp_eq_u32_e32 vcc, v18, v44
	v_add3_u32 v5, v7, v16, v17
	v_mul_f32_e32 v17, 0x39000000, v19
	v_cndmask_b32_e32 v7, 0, v20, vcc
	v_cmp_eq_u32_e32 vcc, v8, v44
	s_nop 1
	v_cndmask_b32_e32 v3, 0, v3, vcc
	v_add3_u32 v5, v5, v7, v3
	v_mul_f32_e32 v3, v4, v19
	v_cvt_f32_i32_e32 v4, v5
	v_mov_b32_e32 v5, 0x2edbe6ff
	v_fmamk_f32 v7, v19, 0x39000000, v5
	v_cmp_gt_f32_e32 vcc, s13, v7
	v_fmac_f32_e32 v5, 0x39000000, v4
	v_mul_f32_e32 v16, 0x39000000, v4
	v_cndmask_b32_e64 v8, 0, 32, vcc
	v_ldexp_f32 v7, v7, v8
	v_log_f32_e32 v7, v7
	s_nop 0
	v_mul_f32_e32 v8, 0x3f317217, v7
	v_fma_f32 v8, v7, s12, -v8
	v_fmac_f32_e32 v8, 0x3377d1cf, v7
	v_fmac_f32_e32 v8, 0x3f317217, v7
	v_cmp_lt_f32_e64 s[2:3], |v7|, s14
	s_nop 1
	v_cndmask_b32_e64 v7, v7, v8, s[2:3]
	v_mov_b32_e32 v8, 0x41b17218
	v_cndmask_b32_e32 v18, 0, v8, vcc
	v_cmp_gt_f32_e32 vcc, s13, v5
	v_sub_f32_e32 v7, v7, v18
	v_cmp_gt_u32_e64 s[2:3], 16, v44
	v_cndmask_b32_e64 v4, 0, 32, vcc
	v_ldexp_f32 v4, v5, v4
	v_log_f32_e32 v4, v4
	v_mul_f32_e32 v5, v17, v7
	v_cndmask_b32_e64 v5, 0, v5, s[2:3]
	ds_bpermute_b32 v17, v11, v5
	v_mul_f32_e32 v7, 0x3f317217, v4
	v_fma_f32 v7, v4, s12, -v7
	v_fmac_f32_e32 v7, 0x3377d1cf, v4
	v_fmac_f32_e32 v7, 0x3f317217, v4
	v_cmp_lt_f32_e64 s[4:5], |v4|, s14
	s_waitcnt lgkmcnt(0)
	v_add_f32_e32 v17, v5, v17
	ds_bpermute_b32 v18, v12, v17
	v_cndmask_b32_e64 v4, v4, v7, s[4:5]
	v_cndmask_b32_e32 v7, 0, v8, vcc
	v_sub_f32_e32 v4, v4, v7
	v_mul_f32_e32 v4, v16, v4
	v_cndmask_b32_e64 v16, 0, v4, s[2:3]
	ds_bpermute_b32 v7, v11, v3
	ds_bpermute_b32 v11, v11, v16
	v_cmp_eq_u32_e32 vcc, 0, v44
	s_waitcnt lgkmcnt(0)
	v_pk_add_f32 v[2:3], v[2:3], v[6:7]
	v_add_f32_e32 v6, v16, v11
	ds_bpermute_b32 v4, v12, v2
	ds_bpermute_b32 v5, v12, v3
	ds_bpermute_b32 v11, v12, v6
	v_add_f32_e32 v7, v17, v18
	ds_bpermute_b32 v12, v13, v7
	s_waitcnt lgkmcnt(0)
	v_pk_add_f32 v[2:3], v[2:3], v[4:5]
	v_add_f32_e32 v6, v6, v11
	ds_bpermute_b32 v4, v13, v2
	ds_bpermute_b32 v5, v13, v3
	ds_bpermute_b32 v11, v13, v6
	v_add_f32_e32 v7, v7, v12
	ds_bpermute_b32 v12, v14, v7
	v_lshlrev_b32_e32 v13, 2, v10
	s_waitcnt lgkmcnt(0)
	v_pk_add_f32 v[2:3], v[2:3], v[4:5]
	v_add_f32_e32 v6, v6, v11
	ds_bpermute_b32 v4, v14, v2
	ds_bpermute_b32 v5, v14, v3
	ds_bpermute_b32 v10, v14, v6
	v_add_f32_e32 v7, v7, v12
	ds_bpermute_b32 v11, v15, v7
	s_waitcnt lgkmcnt(0)
	v_pk_add_f32 v[2:3], v[2:3], v[4:5]
	v_add_f32_e32 v10, v6, v10
	ds_bpermute_b32 v4, v15, v2
	ds_bpermute_b32 v5, v15, v3
	ds_bpermute_b32 v12, v15, v10
	v_add_f32_e32 v7, v7, v11
	ds_bpermute_b32 v6, v13, v9
	ds_bpermute_b32 v11, v13, v7
	s_waitcnt lgkmcnt(0)
	v_pk_add_f32 v[2:3], v[2:3], v[4:5]
	v_add_f32_e32 v10, v10, v12
	ds_bpermute_b32 v4, v13, v2
	ds_bpermute_b32 v5, v13, v3
	ds_bpermute_b32 v12, v13, v10
	s_and_saveexec_b64 s[6:7], vcc
	s_cbranch_execz .LBB4_46
	v_add_f32_e32 v7, v7, v11
	s_waitcnt lgkmcnt(0)
	v_pk_add_f32 v[2:3], v[2:3], v[4:5]
	s_mov_b32 s2, 0xbfb8aa3b
	v_mul_f32_e32 v5, 0xbfb8aa3b, v7
	v_add_f32_e32 v4, v9, v6
	v_fma_f32 v6, v7, s2, -v5
	v_rndne_f32_e32 v9, v5
	v_fmac_f32_e32 v6, 0xb2a5705f, v7
	v_sub_f32_e32 v5, v5, v9
	v_add_f32_e32 v5, v5, v6
	v_exp_f32_e32 v5, v5
	v_cvt_i32_f32_e32 v6, v9
	v_add_f32_e32 v10, v10, v12
	v_add_f32_e32 v2, v2, v3
	s_mov_b32 s3, 0x42ce8ed0
	v_ldexp_f32 v3, v5, v6
	v_mul_f32_e32 v5, 0xbfb8aa3b, v10
	v_fma_f32 v6, v10, s2, -v5
	v_rndne_f32_e32 v9, v5
	v_fmac_f32_e32 v6, 0xb2a5705f, v10
	v_sub_f32_e32 v5, v5, v9
	v_cmp_nlt_f32_e32 vcc, s3, v7
	s_mov_b32 s4, 0xc2b17218
	v_add_f32_e32 v5, v5, v6
	v_cndmask_b32_e32 v3, 0, v3, vcc
	v_exp_f32_e32 v5, v5
	v_cvt_i32_f32_e32 v6, v9
	v_mov_b32_e32 v9, 0x7f800000
	v_cmp_ngt_f32_e32 vcc, s4, v7
	v_cmp_nlt_f32_e64 s[2:3], s3, v10
	v_ldexp_f32 v5, v5, v6
	v_cndmask_b32_e32 v3, v9, v3, vcc
	v_add_f32_e32 v3, 0x2edbe6ff, v3
	v_cmp_gt_f32_e32 vcc, s13, v3
	v_cndmask_b32_e64 v5, 0, v5, s[2:3]
	v_cmp_ngt_f32_e64 s[2:3], s4, v10
	v_cndmask_b32_e64 v6, 0, 32, vcc
	v_ldexp_f32 v3, v3, v6
	v_log_f32_e32 v3, v3
	v_cndmask_b32_e64 v5, v9, v5, s[2:3]
	v_add_f32_e32 v5, 0x2edbe6ff, v5
	v_cmp_gt_f32_e64 s[2:3], s13, v5
	v_mul_f32_e32 v6, 0x3f317217, v3
	v_fma_f32 v6, v3, s12, -v6
	v_cndmask_b32_e64 v7, 0, 32, s[2:3]
	v_ldexp_f32 v5, v5, v7
	v_log_f32_e32 v5, v5
	v_fmac_f32_e32 v6, 0x3377d1cf, v3
	v_fmac_f32_e32 v6, 0x3f317217, v3
	v_cmp_lt_f32_e64 s[4:5], |v3|, s14
	v_mul_f32_e32 v2, 0x3fa00000, v2
	v_mul_f32_e32 v2, 0x34aaaaab, v2
	v_cndmask_b32_e64 v3, v3, v6, s[4:5]
	v_cndmask_b32_e32 v6, 0, v8, vcc
	v_sub_f32_e32 v3, v3, v6
	v_mul_f32_e32 v6, 0x3f317217, v5
	v_fma_f32 v6, v5, s12, -v6
	v_fmac_f32_e32 v6, 0x3377d1cf, v5
	v_fmac_f32_e32 v6, 0x3f317217, v5
	v_cmp_lt_f32_e64 vcc, |v5|, s14
	s_mov_b32 s4, 0x4a400000
	s_nop 0
	v_cndmask_b32_e32 v5, v5, v6, vcc
	v_cndmask_b32_e64 v6, 0, v8, s[2:3]
	v_div_scale_f32 v7, s[2:3], s4, s4, v4
	v_rcp_f32_e32 v8, v7
	v_sub_f32_e32 v5, v5, v6
	v_add_f32_e32 v3, v3, v5
	v_mul_f32_e32 v3, 0xbdcccccd, v3
	v_fma_f32 v5, -v7, v8, 1.0
	v_fmac_f32_e32 v8, v5, v8
	v_div_scale_f32 v5, vcc, v4, s4, v4
	v_mul_f32_e32 v6, v5, v8
	v_fma_f32 v9, -v7, v6, v5
	v_fmac_f32_e32 v6, v9, v8
	v_fma_f32 v5, -v7, v6, v5
	v_div_fmas_f32 v5, v5, v8, v6
	v_div_fixup_f32 v4, v5, s4, v4
	v_mov_b32_e32 v5, 0
	global_store_dwordx3 v5, v[2:4], s[10:11] sc1
